# previous + P4 mixer-post: 36 more ds_bpermute butterfly hops (group-norm/rmsnorm sums) replaced by DPP row ops
# baseline (speedup 1.0000x reference)
; __device__ __forceinline__ void p4_item(Ctx& F, int item) {
;     ...
;     for (int rr = 0; rr < 8; ++rr) {
;         const int t = item * 64 + 8 * w + rr;
;         {
;             float o[16];
; #pragma unroll
;             for (int q = 0; q < 4; ++q) { const f32x4 v = *(const f32x4*)(reto + (size_t)t * RW + c0 + 4 * q); o[4 * q] = v.x; o[4 * q + 1] = v.y; o[4 * q + 2] = v.z; o[4 * q + 3] = v.w; }
;             float s = 0.f;
; #pragma unroll
;             for (int q = 0; q < 16; ++q) s += o[q];
;             s += __shfl_xor(s, 1); s += __shfl_xor(s, 2); s += __shfl_xor(s, 4);
;             const float mu = s * (1.0f / 128.0f); float vq = 0.f;
; #pragma unroll
;             for (int q = 0; q < 16; ++q) { o[q] -= mu; vq += o[q] * o[q]; }
;             vq += __shfl_xor(vq, 1); vq += __shfl_xor(vq, 2); vq += __shfl_xor(vq, 4);
.LBB0_441:
	v_lshl_add_u64 v[38:39], s[96:97], 0, v[76:77]
	v_lshl_add_u64 v[80:81], s[96:97], 0, v[72:73]
	v_lshl_add_u64 v[86:87], v[38:39], 0, s[34:35]
	v_add_co_u32_e32 v38, vcc, 0x3da00000, v38
	v_add_co_u32_e64 v92, s[0:1], s63, v80
	v_lshl_add_u64 v[90:91], v[80:81], 0, s[42:43]
	s_nop 0
	v_addc_co_u32_e64 v93, s[0:1], 0, v81, s[0:1]
	v_addc_co_u32_e32 v39, vcc, 0, v39, vcc
	global_load_dwordx4 v[114:117], v[92:93], off offset:2048
	global_load_dwordx4 v[118:121], v[90:91], off offset:16
	global_load_dwordx4 v[122:125], v[86:87], off offset:32
	global_load_dwordx4 v[126:129], v[86:87], off offset:16
	global_load_dwordx4 v[130:133], v[38:39], off
	global_load_dwordx4 v[134:137], v[86:87], off offset:48
	v_lshl_add_u64 v[82:83], s[96:97], 0, v[74:75]
	v_add_co_u32_e64 v88, s[0:1], s64, v82
	v_lshl_add_u64 v[84:85], s[96:97], 0, v[70:71]
	s_nop 0
	v_addc_co_u32_e64 v89, s[0:1], 0, v83, s[0:1]
	v_add_co_u32_e64 v100, s[0:1], s65, v84
	s_add_i32 s4, s60, s6
	s_nop 0
	v_addc_co_u32_e64 v101, s[0:1], 0, v85, s[0:1]
	v_add_co_u32_e64 v102, s[0:1], s66, v84
	s_ashr_i32 s5, s4, 31
	s_nop 0
	v_addc_co_u32_e64 v103, s[0:1], 0, v85, s[0:1]
	v_add_co_u32_e64 v106, s[0:1], s67, v80
	s_mul_i32 s8, s4, 0x3000
	s_nop 0
	v_addc_co_u32_e64 v107, s[0:1], 0, v81, s[0:1]
	s_lshl_b64 s[0:1], s[4:5], 12
	s_mul_hi_i32 s7, s4, 0x3000
	s_add_u32 s8, s3, s8
	s_addc_u32 s9, s33, s7
	v_lshl_add_u64 v[86:87], s[8:9], 0, v[50:51]
	v_add_co_u32_e32 v94, vcc, s70, v86
	v_lshl_add_u64 v[96:97], v[84:85], 0, s[36:37]
	s_nop 0
	v_addc_co_u32_e32 v95, vcc, 0, v87, vcc
	v_lshl_add_u64 v[98:99], v[84:85], 0, s[38:39]
	v_lshl_add_u64 v[92:93], v[86:87], 0, s[46:47]
	v_lshl_add_u64 v[84:85], v[86:87], 0, s[48:49]
	v_add_co_u32_e32 v86, vcc, s71, v86
	v_lshl_add_u64 v[104:105], v[80:81], 0, s[44:45]
	s_nop 0
	v_addc_co_u32_e32 v87, vcc, 0, v87, vcc
	v_lshl_add_u64 v[90:91], v[60:61], 0, s[0:1]
	v_lshl_add_u64 v[38:39], v[68:69], 0, s[0:1]
	s_lshl_b64 s[0:1], s[4:5], 11
	v_lshl_add_u64 v[80:81], v[64:65], 0, s[0:1]
	v_lshl_add_u64 v[82:83], v[66:67], 0, s[0:1]
	s_add_i32 s6, s6, 2
	v_lshl_add_u64 v[70:71], v[70:71], 0, s[50:51]
	v_lshl_add_u64 v[72:73], v[72:73], 0, s[52:53]
	v_lshl_add_u64 v[74:75], v[74:75], 0, s[54:55]
	v_lshl_add_u64 v[76:77], v[76:77], 0, s[54:55]
	s_cmp_lg_u32 s6, 8
	s_waitcnt vmcnt(4)
	v_and_b32_e32 v152, 0xffff0000, v121
	v_lshlrev_b32_e32 v138, 16, v114
	s_waitcnt vmcnt(1)
	v_add_f32_e32 v113, 0, v130
	v_add_f32_e32 v113, v131, v113
	v_add_f32_e32 v113, v132, v113
	v_add_f32_e32 v113, v133, v113
	v_add_f32_e32 v113, v126, v113
	v_add_f32_e32 v113, v127, v113
	v_add_f32_e32 v113, v128, v113
	v_add_f32_e32 v113, v129, v113
	v_add_f32_e32 v113, v122, v113
	v_add_f32_e32 v113, v123, v113
	v_mul_f32_e32 v139, 0xbfb8aa3b, v138
	v_add_f32_e32 v113, v124, v113
	v_mul_f32_e32 v154, 0xbfb8aa3b, v152
	v_exp_f32_e32 v139, v139
	v_add_f32_e32 v113, v125, v113
	v_exp_f32_e32 v154, v154
	s_waitcnt vmcnt(0)
	v_add_f32_e32 v113, v134, v113
	v_add_f32_e32 v113, v135, v113
	v_add_f32_e32 v113, v136, v113
	v_add_f32_e32 v139, 1.0, v139
	v_add_f32_e32 v113, v137, v113
	v_add_f32_e32 v170, 1.0, v154
	v_rcp_f32_e32 v154, v139
	v_and_b32_e32 v140, 0xffff0000, v114
	v_and_b32_e32 v114, 0xffff0000, v115
	v_and_b32_e32 v146, 0xffff0000, v118
	v_and_b32_e32 v148, 0xffff0000, v119
	s_waitcnt lgkmcnt(0)
	s_nop 1
	v_add_f32_dpp v113, v113, v113 quad_perm:[1,0,3,2] row_mask:0xf bank_mask:0xf
	v_and_b32_e32 v150, 0xffff0000, v120
	v_mul_f32_e32 v141, 0xbfb8aa3b, v140
	v_mul_f32_e32 v143, 0xbfb8aa3b, v114
	v_mul_f32_e32 v149, 0xbfb8aa3b, v146
	s_waitcnt lgkmcnt(0)
	s_nop 1
	v_add_f32_dpp v113, v113, v113 quad_perm:[2,3,0,1] row_mask:0xf bank_mask:0xf
	v_mul_f32_e32 v151, 0xbfb8aa3b, v148
	v_mul_f32_e32 v153, 0xbfb8aa3b, v150
	v_exp_f32_e32 v141, v141
	v_exp_f32_e32 v143, v143
	s_waitcnt lgkmcnt(0)
	s_nop 1
	v_add_f32_dpp v113, v113, v113 row_half_mirror row_mask:0xf bank_mask:0xf
	v_fmamk_f32 v157, v113, 0xbc000000, v131
	v_mul_f32_e32 v160, 0x3c000000, v113
	v_fmamk_f32 v155, v113, 0xbc000000, v130
	v_fmamk_f32 v131, v113, 0xbc000000, v132
	v_fmac_f32_e32 v133, 0xbc000000, v113
	v_fmamk_f32 v161, v113, 0xbc000000, v126
	v_fmamk_f32 v159, v113, 0xbc000000, v127
	v_fmamk_f32 v127, v113, 0xbc000000, v128
	v_fmac_f32_e32 v129, 0xbc000000, v113
	v_mul_f32_e32 v113, v157, v157
	v_fmac_f32_e32 v113, v155, v155
	v_fmac_f32_e32 v113, v131, v131
	v_fmac_f32_e32 v113, v133, v133
	v_fmac_f32_e32 v113, v161, v161
	v_fmac_f32_e32 v113, v159, v159
	v_pk_add_f32 v[122:123], v[122:123], v[160:161] op_sel_hi:[1,0] neg_lo:[0,1] neg_hi:[0,1]
	v_fmac_f32_e32 v113, v127, v127
	v_pk_mul_f32 v[162:163], v[122:123], v[122:123]
	v_fmac_f32_e32 v113, v129, v129
	v_pk_add_f32 v[124:125], v[124:125], v[160:161] op_sel_hi:[1,0] neg_lo:[0,1] neg_hi:[0,1]
	v_add_f32_e32 v113, v162, v113
	v_pk_mul_f32 v[164:165], v[124:125], v[124:125]
	v_add_f32_e32 v113, v163, v113
	v_pk_add_f32 v[134:135], v[134:135], v[160:161] op_sel_hi:[1,0] neg_lo:[0,1] neg_hi:[0,1]
	v_add_f32_e32 v113, v164, v113
	v_pk_mul_f32 v[166:167], v[134:135], v[134:135]
	v_add_f32_e32 v113, v165, v113
	v_pk_add_f32 v[136:137], v[136:137], v[160:161] op_sel_hi:[1,0] neg_lo:[0,1] neg_hi:[0,1]
	v_add_f32_e32 v113, v166, v113
	v_pk_mul_f32 v[168:169], v[136:137], v[136:137]
	v_add_f32_e32 v113, v167, v113
	v_add_f32_e32 v113, v168, v113
	v_add_f32_e32 v113, v169, v113
	v_exp_f32_e32 v149, v149
	v_exp_f32_e32 v151, v151
	v_exp_f32_e32 v153, v153
	v_and_b32_e32 v144, 0xffff0000, v117
	s_waitcnt lgkmcnt(0)
	s_nop 1
	v_add_f32_dpp v113, v113, v113 quad_perm:[1,0,3,2] row_mask:0xf bank_mask:0xf
	v_mul_f32_e32 v147, 0xbfb8aa3b, v144
	v_exp_f32_e32 v147, v147
	v_add_f32_e32 v141, 1.0, v141
	v_add_f32_e32 v143, 1.0, v143
	s_waitcnt lgkmcnt(0)
; __device__ __forceinline__ float bflo(unsigned w) { return __uint_as_float(w << 16); }
; __device__ __forceinline__ float bfhi(unsigned w) { return __uint_as_float(w & 0xffff0000u); }
; __device__ __forceinline__ float siluf_(float x) { return x * __builtin_amdgcn_rcpf(1.0f + __expf(-x)); }
; __device__ __forceinline__ void p4_item(Ctx& F, int item) {
;     ...
;             for (int q = 0; q < 16; ++q) { o[q] -= mu; vq += o[q] * o[q]; }
;             vq += __shfl_xor(vq, 1); vq += __shfl_xor(vq, 2); vq += __shfl_xor(vq, 4);
;             const float rs = rsqrtf(vq * (1.0f / 128.0f) + EPS);
;             const u32x4 g0 = *(const u32x4*)(proj + (size_t)t * NIN + 3 * RW + c0), g1 = *(const u32x4*)(proj + (size_t)t * NIN + 3 * RW + c0 + 8);
;             float ss = 0.f;
; #pragma unroll
;             for (int q = 0; q < 8; ++q) { const unsigned gw_ = (q < 4) ? g0[q & 3] : g1[q & 3]; const float ga = bflo(gw_), gb = bfhi(gw_);
;                 o[2 * q] = siluf_(ga) * (o[2 * q] * rs); o[2 * q + 1] = siluf_(gb) * (o[2 * q + 1] * rs); ss += o[2 * q] * o[2 * q] + o[2 * q + 1] * o[2 * q + 1]; }
;             const float rstd = rsqrtf(wave_sum(ss) * (1.0f / RW) + EPS);
	s_nop 1
	v_add_f32_dpp v113, v113, v113 quad_perm:[2,3,0,1] row_mask:0xf bank_mask:0xf
	v_add_f32_e32 v149, 1.0, v149
	v_add_f32_e32 v151, 1.0, v151
	v_add_f32_e32 v153, 1.0, v153
	v_rcp_f32_e32 v156, v141
	s_waitcnt lgkmcnt(0)
	s_nop 1
	v_add_f32_dpp v113, v113, v113 row_half_mirror row_mask:0xf bank_mask:0xf
	v_fmamk_f32 v113, v113, 0x3c000000, v112
	v_mul_f32_e32 v126, 0x4b800000, v113
	v_cmp_gt_f32_e32 vcc, s62, v113
	v_rcp_f32_e32 v132, v143
	v_mov_b32_e32 v171, v122
	v_cndmask_b32_e32 v113, v113, v126, vcc
	v_rsq_f32_e32 v113, v113
	v_rcp_f32_e32 v122, v149
	v_mov_b32_e32 v173, v124
	v_rcp_f32_e32 v124, v151
	v_mul_f32_e32 v126, 0x45800000, v113
	v_cndmask_b32_e32 v139, v113, v126, vcc
	v_mov_b32_e32 v175, v134
	v_rcp_f32_e32 v134, v153
	v_mov_b32_e32 v177, v136
	v_rcp_f32_e32 v136, v170
	v_pk_mul_f32 v[154:155], v[154:155], v[138:139]
	v_lshlrev_b32_e32 v138, 16, v115
	v_mul_f32_e32 v126, 0xbfb8aa3b, v138
	v_add_f32_e32 v147, 1.0, v147
	v_exp_f32_e32 v126, v126
	v_rcp_f32_e32 v128, v147
	v_mov_b32_e32 v141, v139
	v_mov_b32_e32 v115, v139
	v_mov_b32_e32 v147, v139
	v_mov_b32_e32 v149, v139
	v_mov_b32_e32 v151, v139
	v_mov_b32_e32 v153, v139
	v_pk_mul_f32 v[140:141], v[156:157], v[140:141]
	v_pk_mul_f32 v[114:115], v[132:133], v[114:115]
	v_pk_mul_f32 v[122:123], v[122:123], v[146:147]
	v_pk_mul_f32 v[124:125], v[124:125], v[148:149]
	v_pk_mul_f32 v[134:135], v[134:135], v[150:151]
	v_pk_mul_f32 v[136:137], v[136:137], v[152:153]
	v_mul_f32_e32 v140, v140, v141
	v_mul_f32_e32 v141, v114, v115
	v_mov_b32_e32 v114, v124
	v_mov_b32_e32 v115, v122
	v_mov_b32_e32 v122, v125
	v_mov_b32_e32 v124, v136
	v_mov_b32_e32 v125, v134
	v_mov_b32_e32 v134, v137
	v_pk_mul_f32 v[114:115], v[114:115], v[122:123]
	v_pk_mul_f32 v[122:123], v[124:125], v[134:135]
	v_add_f32_e32 v124, 1.0, v126
	v_rcp_f32_e32 v130, v124
	v_and_b32_e32 v142, 0xffff0000, v116
	v_mul_f32_e32 v145, 0xbfb8aa3b, v142
	v_exp_f32_e32 v145, v145
	v_pk_mul_f32 v[124:125], v[130:131], v[138:139]
	v_lshlrev_b32_e32 v138, 16, v116
	v_mul_f32_e32 v116, 0xbfb8aa3b, v138
	v_exp_f32_e32 v116, v116
	v_add_f32_e32 v145, 1.0, v145
	v_rcp_f32_e32 v158, v145
	v_mul_f32_e32 v130, v124, v125
	v_add_f32_e32 v116, 1.0, v116
	v_rcp_f32_e32 v160, v116
	v_mov_b32_e32 v143, v139
	v_mov_b32_e32 v145, v139
	v_pk_mul_f32 v[132:133], v[158:159], v[142:143]
	v_pk_mul_f32 v[124:125], v[160:161], v[138:139]
	v_lshlrev_b32_e32 v138, 16, v117
	v_mul_f32_e32 v116, 0xbfb8aa3b, v138
	v_pk_mul_f32 v[128:129], v[128:129], v[144:145]
	v_exp_f32_e32 v116, v116
	v_mul_f32_e32 v113, v154, v155
	v_mul_f32_e32 v132, v132, v133
	v_mul_f32_e32 v128, v128, v129
	v_mul_f32_e32 v129, v141, v141
	v_mul_f32_e32 v133, v140, v140
	v_fmac_f32_e32 v133, v113, v113
	v_fmac_f32_e32 v129, v130, v130
	v_mul_f32_e32 v134, v132, v132
	v_add_f32_e32 v126, v133, v129
	v_mul_f32_e32 v129, v124, v125
	v_fmac_f32_e32 v134, v129, v129
	v_add_f32_e32 v116, 1.0, v116
	v_add_f32_e32 v124, v134, v126
	v_rcp_f32_e32 v126, v116
	v_mul_f32_e32 v135, v128, v128
	v_pk_mul_f32 v[116:117], v[126:127], v[138:139]
	v_lshlrev_b32_e32 v138, 16, v118
	v_mul_f32_e32 v126, v116, v117
	v_mul_f32_e32 v116, 0xbfb8aa3b, v138
	v_exp_f32_e32 v116, v116
	v_fmac_f32_e32 v135, v126, v126
	v_add_f32_e32 v127, v135, v124
	v_add_f32_e32 v116, 1.0, v116
	v_rcp_f32_e32 v170, v116
	s_nop 0
	v_pk_mul_f32 v[116:117], v[170:171], v[138:139]
	v_lshlrev_b32_e32 v138, 16, v119
	v_mul_f32_e32 v118, 0xbfb8aa3b, v138
	v_mov_b32_e32 v119, v116
	v_exp_f32_e32 v116, v118
	s_nop 0
	v_add_f32_e32 v116, 1.0, v116
	v_rcp_f32_e32 v172, v116
	s_nop 0
	v_pk_mul_f32 v[124:125], v[172:173], v[138:139]
	v_lshlrev_b32_e32 v138, 16, v120
	v_mul_f32_e32 v120, 0xbfb8aa3b, v138
	v_exp_f32_e32 v120, v120
	v_mov_b32_e32 v118, v124
	v_mov_b32_e32 v116, v125
	v_pk_mul_f32 v[116:117], v[118:119], v[116:117]
	v_add_f32_e32 v120, 1.0, v120
	v_rcp_f32_e32 v174, v120
	v_pk_mul_f32 v[118:119], v[116:117], v[116:117]
	s_nop 0
	v_pk_fma_f32 v[118:119], v[114:115], v[114:115], v[118:119]
	s_nop 0
	v_add_f32_e32 v119, v119, v127
	v_add_f32_e32 v127, v118, v119
	v_pk_mul_f32 v[118:119], v[174:175], v[138:139]
	v_lshlrev_b32_e32 v138, 16, v121
	v_mul_f32_e32 v120, 0xbfb8aa3b, v138
	v_mov_b32_e32 v121, v118
	v_exp_f32_e32 v118, v120
	s_nop 0
	v_add_f32_e32 v118, 1.0, v118
	v_rcp_f32_e32 v176, v118
	s_nop 0
	v_pk_mul_f32 v[124:125], v[176:177], v[138:139]
	s_nop 0
	v_mov_b32_e32 v120, v124
	v_mov_b32_e32 v118, v125
	v_pk_mul_f32 v[118:119], v[120:121], v[118:119]
	s_nop 0
	v_pk_mul_f32 v[120:121], v[118:119], v[118:119]
	s_nop 0
	v_pk_fma_f32 v[120:121], v[122:123], v[122:123], v[120:121]
	s_nop 0
	v_add_f32_e32 v121, v121, v127
	v_add_f32_e32 v120, v120, v121
	s_waitcnt lgkmcnt(0)
	s_nop 1
	v_add_f32_dpp v120, v120, v120 quad_perm:[1,0,3,2] row_mask:0xf bank_mask:0xf
	s_waitcnt lgkmcnt(0)
	s_nop 1
	v_add_f32_dpp v120, v120, v120 quad_perm:[2,3,0,1] row_mask:0xf bank_mask:0xf
	s_waitcnt lgkmcnt(0)
	s_nop 1
	v_add_f32_dpp v120, v120, v120 row_half_mirror row_mask:0xf bank_mask:0xf
	s_waitcnt lgkmcnt(0)
	s_nop 1
	v_add_f32_dpp v120, v120, v120 row_mirror row_mask:0xf bank_mask:0xf
	s_waitcnt lgkmcnt(0)
	s_nop 1
	v_add_f32_dpp v120, v120, v120 row_bcast:15 row_mask:0xa bank_mask:0xf
	s_waitcnt lgkmcnt(0)
; __device__ __forceinline__ unsigned pk2(float lo, float hi) { unsigned r; asm volatile("v_cvt_pk_bf16_f32 %0, %1, %2" : "=v"(r) : "v"(lo), "v"(hi)); return r; }
; __device__ __forceinline__ float bflo(unsigned w) { return __uint_as_float(w << 16); }
; __device__ __forceinline__ float bfhi(unsigned w) { return __uint_as_float(w & 0xffff0000u); }
; __device__ __forceinline__ float gelu_tanh_(float x) { const float u = 0.7978845608028654f * (x + 0.044715f * x * x * x); const float e = __expf(2.0f * u); const float th = 1.0f - 2.0f * __builtin_amdgcn_rcpf(e + 1.0f); return 0.5f * x * (1.0f + th); }
; __device__ __forceinline__ void p4_item(Ctx& F, int item) {
;     ...
;             const float rstd = rsqrtf(wave_sum(ss) * (1.0f / RW) + EPS);
;             u32x4 w0, w1;
; #pragma unroll
;             for (int q = 0; q < 4; ++q) { w0[q] = pk2(o[2 * q] * rstd * beta_r[2 * q], o[2 * q + 1] * rstd * beta_r[2 * q + 1]); w1[q] = pk2(o[8 + 2 * q] * rstd * beta_r[8 + 2 * q], o[9 + 2 * q] * rstd * beta_r[9 + 2 * q]); }
;             *(u32x4*)(cat + (size_t)t * DM + c0) = w0; *(u32x4*)(cat + (size_t)t * DM + c0 + 8) = w1;
;         }
;         {
;             const u32x4 h0 = *(const u32x4*)(hl + (size_t)t * LW + c0), h1 = *(const u32x4*)(hl + (size_t)t * LW + c0 + 8), p0 = *(const u32x4*)(pl + (size_t)t * LW + c0), p1 = *(const u32x4*)(pl + (size_t)t * LW + c0 + 8);
;             const u32x4 y0 = *(const u32x4*)(proj + (size_t)t * NIN + 5 * RW + c0), y1 = *(const u32x4*)(proj + (size_t)t * NIN + 5 * RW + c0 + 8);
;             float o[16]; float ss = 0.f;
; #pragma unroll
;             for (int q = 0; q < 8; ++q) { const unsigned hw = (q < 4) ? h0[q & 3] : h1[q & 3], pw = (q < 4) ? p0[q & 3] : p1[q & 3], yw = (q < 4) ? y0[q & 3] : y1[q & 3];
;                 const float ha = bflo(hw) + bflo(pw) * cr[2 * q], hb = bfhi(hw) + bfhi(pw) * cr[2 * q + 1];
;                 o[2 * q] = ha * gelu_tanh_(bflo(yw)); o[2 * q + 1] = hb * gelu_tanh_(bfhi(yw)); ss += o[2 * q] * o[2 * q] + o[2 * q + 1] * o[2 * q + 1]; }
	s_nop 1
	v_add_f32_dpp v120, v120, v120 row_bcast:31 row_mask:0xc bank_mask:0xf
	s_nop 1
	v_readlane_b32 s98, v120, 63
	s_nop 1
	v_mov_b32_e32 v120, s98
	v_fmamk_f32 v120, v120, 0x3a800000, v112
	v_mul_f32_e32 v121, 0x4b800000, v120
	v_cmp_gt_f32_e32 vcc, s62, v120
	s_nop 1
	v_cndmask_b32_e32 v120, v120, v121, vcc
	v_rsq_f32_e32 v120, v120
	s_nop 0
	v_mul_f32_e32 v121, 0x45800000, v120
	v_cndmask_b32_e32 v120, v120, v121, vcc
	v_mul_f32_e32 v117, v117, v120
	v_mul_f32_e32 v115, v115, v120
	v_mul_f32_e32 v116, v116, v120
	v_mul_f32_e32 v113, v113, v120
	v_mul_f32_e32 v121, v140, v120
	v_mul_f32_e32 v124, v130, v120
	v_mul_f32_e32 v125, v141, v120
	v_mul_f32_e32 v114, v114, v120
	v_mul_f32_e32 v127, v129, v120
	v_mul_f32_e32 v129, v132, v120
	v_mul_f32_e32 v119, v119, v120
	v_mul_f32_e32 v123, v123, v120
	v_mul_f32_e32 v126, v126, v120
	v_mul_f32_e32 v128, v128, v120
	v_mul_f32_e32 v118, v118, v120
	v_mul_f32_e32 v120, v122, v120
	v_mul_f32_e32 v117, v10, v117
	v_mul_f32_e32 v115, v11, v115
	v_mul_f32_e32 v116, v12, v116
	v_mul_f32_e32 v113, v2, v113
	v_mul_f32_e32 v121, v3, v121
	v_mul_f32_e32 v122, v4, v124
	v_mul_f32_e32 v124, v5, v125
	v_mul_f32_e32 v125, v13, v114
	v_mul_f32_e32 v127, v6, v127
	v_mul_f32_e32 v129, v7, v129
	v_mul_f32_e32 v130, v14, v119
	v_mul_f32_e32 v123, v15, v123
	v_mul_f32_e32 v126, v8, v126
	v_mul_f32_e32 v128, v9, v128
	v_mul_f32_e32 v131, v16, v118
	v_mul_f32_e32 v132, v17, v120
	v_cvt_pk_bf16_f32 v114, v113, v121
	v_cvt_pk_bf16_f32 v118, v117, v115
	v_cvt_pk_bf16_f32 v115, v122, v124
	v_cvt_pk_bf16_f32 v119, v116, v125
	v_cvt_pk_bf16_f32 v116, v127, v129
	v_cvt_pk_bf16_f32 v120, v130, v123
	v_cvt_pk_bf16_f32 v117, v126, v128
	v_cvt_pk_bf16_f32 v121, v131, v132
	global_store_dwordx4 v[88:89], v[114:117], off
	global_store_dwordx4 v[88:89], v[118:121], off offset:16
	global_load_dwordx4 v[114:117], v[100:101], off
	s_nop 0
	global_load_dwordx4 v[100:103], v[102:103], off
	s_nop 0
	global_load_dwordx4 v[118:121], v[106:107], off offset:2048
	s_nop 0
	global_load_dwordx4 v[104:107], v[104:105], off offset:16
	s_nop 0
	global_load_dwordx4 v[122:125], v[96:97], off offset:16
	s_nop 0
	global_load_dwordx4 v[96:99], v[98:99], off offset:16
	s_waitcnt vmcnt(5)
	v_lshlrev_b32_e32 v113, 16, v114
	s_waitcnt vmcnt(4)
	v_lshlrev_b32_e32 v126, 16, v100
	s_waitcnt vmcnt(3)
	v_lshlrev_b32_e32 v129, 16, v118
	v_and_b32_e32 v130, 0xffff0000, v118
	v_lshlrev_b32_e32 v131, 16, v115
	v_lshlrev_b32_e32 v132, 16, v101
	v_lshlrev_b32_e32 v135, 16, v119
	v_and_b32_e32 v136, 0xffff0000, v119
	v_and_b32_e32 v128, 0xffff0000, v100
	v_and_b32_e32 v134, 0xffff0000, v101
	v_lshlrev_b32_e32 v137, 16, v116
	v_lshlrev_b32_e32 v138, 16, v102
	v_and_b32_e32 v140, 0xffff0000, v102
	v_lshlrev_b32_e32 v141, 16, v120
	v_and_b32_e32 v142, 0xffff0000, v120
	v_lshlrev_b32_e32 v143, 16, v117
	v_lshlrev_b32_e32 v144, 16, v103
	v_and_b32_e32 v146, 0xffff0000, v103
	v_lshlrev_b32_e32 v147, 16, v121
	v_and_b32_e32 v148, 0xffff0000, v121
	s_waitcnt vmcnt(2)
	v_lshlrev_b32_e32 v101, 16, v105
	v_lshlrev_b32_e32 v100, 16, v104
	v_and_b32_e32 v103, 0xffff0000, v105
	v_and_b32_e32 v102, 0xffff0000, v104
	v_lshlrev_b32_e32 v119, 16, v107
	v_lshlrev_b32_e32 v118, 16, v106
	v_and_b32_e32 v107, 0xffff0000, v107
	v_and_b32_e32 v106, 0xffff0000, v106
	v_fmac_f32_e32 v113, v42, v126
	v_mul_f32_e32 v126, 0x3d372713, v129
	v_mul_f32_e32 v149, 0x3d372713, v130
	v_fmac_f32_e32 v131, v44, v132
	v_mul_f32_e32 v132, 0x3d372713, v135
	v_mul_f32_e32 v151, 0x3d372713, v136
	v_and_b32_e32 v127, 0xffff0000, v114
	v_and_b32_e32 v133, 0xffff0000, v115
	v_and_b32_e32 v139, 0xffff0000, v116
	v_and_b32_e32 v145, 0xffff0000, v117
	s_waitcnt vmcnt(1)
	v_lshlrev_b32_e32 v105, 16, v123
	v_lshlrev_b32_e32 v104, 16, v122
	s_waitcnt vmcnt(0)
	v_lshlrev_b32_e32 v115, 16, v97
	v_lshlrev_b32_e32 v114, 16, v96
	v_and_b32_e32 v117, 0xffff0000, v123
	v_and_b32_e32 v116, 0xffff0000, v122
	v_and_b32_e32 v97, 0xffff0000, v97
	v_and_b32_e32 v96, 0xffff0000, v96
	v_lshlrev_b32_e32 v121, 16, v125
	v_lshlrev_b32_e32 v120, 16, v124
	v_lshlrev_b32_e32 v123, 16, v99
	v_lshlrev_b32_e32 v122, 16, v98
	v_and_b32_e32 v125, 0xffff0000, v125
	v_and_b32_e32 v124, 0xffff0000, v124
	v_and_b32_e32 v99, 0xffff0000, v99
	v_and_b32_e32 v98, 0xffff0000, v98
	v_fmac_f32_e32 v137, v46, v138
	v_mul_f32_e32 v138, 0x3d372713, v141
	v_mul_f32_e32 v153, 0x3d372713, v142
	v_fmac_f32_e32 v143, v48, v144
	v_mul_f32_e32 v144, 0x3d372713, v147
	v_mul_f32_e32 v155, 0x3d372713, v148
	v_mul_f32_e32 v157, 0x3d372713, v100
	v_mul_f32_e32 v159, 0x3d372713, v102
	v_mul_f32_e32 v161, 0x3d372713, v101
	v_mul_f32_e32 v163, 0x3d372713, v103
	v_mul_f32_e32 v167, 0x3d372713, v106
	v_mul_f32_e32 v171, 0x3d372713, v107
	v_mul_f32_e32 v126, v126, v129
	v_mul_f32_e32 v149, v149, v130
	v_mul_f32_e32 v132, v132, v135
	v_mul_f32_e32 v151, v151, v136
	v_fmac_f32_e32 v127, v43, v128
	v_mul_f32_e32 v128, 0.5, v129
	v_mul_f32_e32 v150, 0.5, v130
	v_mov_b32_e32 v158, v100
	v_mov_b32_e32 v160, v102
	v_pk_fma_f32 v[104:105], v[34:35], v[114:115], v[104:105]
	v_pk_fma_f32 v[96:97], v[40:41], v[96:97], v[116:117]
	v_mov_b32_e32 v162, v101
	v_pk_mul_f32 v[114:115], v[100:101], 0.5 op_sel_hi:[1,0]
	v_mov_b32_e32 v164, v103
	v_pk_mul_f32 v[116:117], v[102:103], 0.5 op_sel_hi:[1,0]
	v_mul_f32_e32 v165, 0x3d372713, v118
	v_mov_b32_e32 v168, v106
	v_pk_fma_f32 v[98:99], v[36:37], v[98:99], v[124:125]
	v_mul_f32_e32 v169, 0x3d372713, v119
	v_mov_b32_e32 v172, v107
	v_pk_mul_f32 v[124:125], v[106:107], 0.5 op_sel_hi:[1,0]
	v_mul_f32_e32 v138, v138, v141
	v_mul_f32_e32 v153, v153, v142
	v_mul_f32_e32 v144, v144, v147
	v_mul_f32_e32 v155, v155, v148
	v_mul_f32_e32 v100, v157, v100
; __device__ __forceinline__ float bflo(unsigned w) { return __uint_as_float(w << 16); }
; __device__ __forceinline__ float bfhi(unsigned w) { return __uint_as_float(w & 0xffff0000u); }
; __device__ __forceinline__ float gelu_tanh_(float x) { const float u = 0.7978845608028654f * (x + 0.044715f * x * x * x); const float e = __expf(2.0f * u); const float th = 1.0f - 2.0f * __builtin_amdgcn_rcpf(e + 1.0f); return 0.5f * x * (1.0f + th); }
; __device__ __forceinline__ void p4_item(Ctx& F, int item) {
;     ...
;             for (int q = 0; q < 8; ++q) { const unsigned hw = (q < 4) ? h0[q & 3] : h1[q & 3], pw = (q < 4) ? p0[q & 3] : p1[q & 3], yw = (q < 4) ? y0[q & 3] : y1[q & 3];
;                 const float ha = bflo(hw) + bflo(pw) * cr[2 * q], hb = bfhi(hw) + bfhi(pw) * cr[2 * q + 1];
;                 o[2 * q] = ha * gelu_tanh_(bflo(yw)); o[2 * q + 1] = hb * gelu_tanh_(bfhi(yw)); ss += o[2 * q] * o[2 * q] + o[2 * q + 1] * o[2 * q + 1]; }
;             const float rstd = rsqrtf(wave_sum(ss) * (1.0f / LW) + EPS);
	v_mul_f32_e32 v102, v159, v102
	v_mul_f32_e32 v101, v161, v101
	v_mul_f32_e32 v103, v163, v103
	v_mul_f32_e32 v106, v167, v106
	v_mul_f32_e32 v107, v171, v107
	v_fma_f32 v126, v126, v129, v129
	v_fma_f32 v129, v149, v130, v130
	v_fma_f32 v130, v132, v135, v135
	v_fma_f32 v132, v151, v136, v136
	v_fmac_f32_e32 v133, v45, v134
	v_mul_f32_e32 v134, 0.5, v135
	v_mul_f32_e32 v152, 0.5, v136
	v_fmac_f32_e32 v139, v47, v140
	v_mul_f32_e32 v140, 0.5, v141
	v_mov_b32_e32 v166, v118
	v_pk_fma_f32 v[120:121], v[78:79], v[122:123], v[120:121]
	v_mov_b32_e32 v170, v119
	v_pk_mul_f32 v[122:123], v[118:119], 0.5 op_sel_hi:[1,0]
	v_mul_f32_e32 v118, v165, v118
	v_mul_f32_e32 v119, v169, v119
	v_fma_f32 v135, v138, v141, v141
	v_fma_f32 v136, v153, v142, v142
	v_fma_f32 v138, v144, v147, v147
	v_fma_f32 v141, v155, v148, v148
	v_fmac_f32_e32 v158, v100, v158
	v_fmac_f32_e32 v160, v102, v160
	v_fmac_f32_e32 v162, v101, v162
	v_fmac_f32_e32 v164, v103, v164
	v_fmac_f32_e32 v168, v106, v168
	v_fmac_f32_e32 v172, v107, v172
	v_mul_f32_e32 v100, 0x3f4c422a, v126
	v_mul_f32_e32 v101, 0x3f4c422a, v129
	v_mul_f32_e32 v102, 0x3f4c422a, v130
	v_mul_f32_e32 v103, 0x3f4c422a, v132
	v_fmac_f32_e32 v166, v118, v166
	v_fmac_f32_e32 v170, v119, v170
	v_mul_f32_e32 v107, 0x3f4c422a, v136
	v_mul_f32_e32 v118, 0x3f4c422a, v138
	v_mul_f32_e32 v119, 0x3f4c422a, v141
	v_mul_f32_e32 v126, 0x3f4c422a, v158
	v_mul_f32_e32 v129, 0x3f4c422a, v160
	v_mul_f32_e32 v130, 0x3f4c422a, v162
	v_mul_f32_e32 v132, 0x3f4c422a, v164
	v_mul_f32_e32 v136, 0x3f4c422a, v168
	v_mul_f32_e32 v141, 0x3f4c422a, v172
	v_add_f32_e32 v100, v100, v100
	v_add_f32_e32 v101, v101, v101
	v_add_f32_e32 v102, v102, v102
	v_add_f32_e32 v103, v103, v103
	v_mul_f32_e32 v106, 0x3f4c422a, v135
	v_mul_f32_e32 v135, 0x3f4c422a, v166
	v_mul_f32_e32 v138, 0x3f4c422a, v170
	v_add_f32_e32 v107, v107, v107
	v_add_f32_e32 v118, v118, v118
	v_add_f32_e32 v119, v119, v119
	v_add_f32_e32 v126, v126, v126
	v_add_f32_e32 v129, v129, v129
	v_add_f32_e32 v130, v130, v130
	v_add_f32_e32 v132, v132, v132
	v_add_f32_e32 v136, v136, v136
	v_add_f32_e32 v141, v141, v141
	v_mul_f32_e32 v100, 0x3fb8aa3b, v100
	v_mul_f32_e32 v101, 0x3fb8aa3b, v101
	v_mul_f32_e32 v102, 0x3fb8aa3b, v102
	v_mul_f32_e32 v103, 0x3fb8aa3b, v103
	v_add_f32_e32 v106, v106, v106
	v_add_f32_e32 v135, v135, v135
	v_add_f32_e32 v138, v138, v138
	v_mul_f32_e32 v107, 0x3fb8aa3b, v107
	v_mul_f32_e32 v118, 0x3fb8aa3b, v118
	v_mul_f32_e32 v119, 0x3fb8aa3b, v119
	v_mul_f32_e32 v126, 0x3fb8aa3b, v126
	v_mul_f32_e32 v129, 0x3fb8aa3b, v129
	v_mul_f32_e32 v130, 0x3fb8aa3b, v130
	v_mul_f32_e32 v132, 0x3fb8aa3b, v132
	v_mul_f32_e32 v136, 0x3fb8aa3b, v136
	v_mul_f32_e32 v141, 0x3fb8aa3b, v141
	v_exp_f32_e32 v100, v100
	v_exp_f32_e32 v101, v101
	v_exp_f32_e32 v102, v102
	v_exp_f32_e32 v103, v103
	v_mul_f32_e32 v106, 0x3fb8aa3b, v106
	v_mul_f32_e32 v135, 0x3fb8aa3b, v135
	v_mul_f32_e32 v138, 0x3fb8aa3b, v138
	v_exp_f32_e32 v107, v107
	v_exp_f32_e32 v118, v118
	v_exp_f32_e32 v119, v119
	v_exp_f32_e32 v126, v126
	v_exp_f32_e32 v129, v129
	v_exp_f32_e32 v130, v130
	v_exp_f32_e32 v132, v132
	v_exp_f32_e32 v136, v136
	v_exp_f32_e32 v141, v141
	v_exp_f32_e32 v106, v106
	v_exp_f32_e32 v135, v135
	v_exp_f32_e32 v138, v138
	v_add_f32_e32 v100, 1.0, v100
	v_add_f32_e32 v101, 1.0, v101
	v_add_f32_e32 v102, 1.0, v102
	v_add_f32_e32 v103, 1.0, v103
	v_mul_f32_e32 v154, 0.5, v142
	v_fmac_f32_e32 v145, v49, v146
	v_mul_f32_e32 v146, 0.5, v147
	v_mul_f32_e32 v156, 0.5, v148
	v_add_f32_e32 v107, 1.0, v107
	v_add_f32_e32 v118, 1.0, v118
	v_add_f32_e32 v119, 1.0, v119
	v_add_f32_e32 v126, 1.0, v126
	v_add_f32_e32 v129, 1.0, v129
	v_add_f32_e32 v130, 1.0, v130
	v_add_f32_e32 v132, 1.0, v132
	v_add_f32_e32 v136, 1.0, v136
	v_add_f32_e32 v141, 1.0, v141
	v_rcp_f32_e32 v142, v100
	v_rcp_f32_e32 v144, v101
	v_rcp_f32_e32 v147, v102
	v_rcp_f32_e32 v148, v103
	v_add_f32_e32 v106, 1.0, v106
	v_add_f32_e32 v135, 1.0, v135
	v_add_f32_e32 v138, 1.0, v138
	v_rcp_f32_e32 v151, v107
	v_rcp_f32_e32 v153, v118
	v_rcp_f32_e32 v155, v119
	v_rcp_f32_e32 v100, v126
	v_rcp_f32_e32 v102, v129
	v_rcp_f32_e32 v101, v130
	v_rcp_f32_e32 v103, v132
	v_rcp_f32_e32 v118, v136
	v_rcp_f32_e32 v119, v141
	v_rcp_f32_e32 v149, v106
	v_rcp_f32_e32 v106, v135
	v_rcp_f32_e32 v107, v138
	v_fma_f32 v126, v142, -2.0, 1.0
	v_fma_f32 v129, v144, -2.0, 1.0
	v_fma_f32 v130, v147, -2.0, 1.0
	v_fma_f32 v132, v148, -2.0, 1.0
	v_fma_f32 v136, v151, -2.0, 1.0
	v_pk_fma_f32 v[100:101], v[100:101], 2.0, 1.0 op_sel_hi:[1,0,0] neg_lo:[1,0,0] neg_hi:[1,0,0]
	v_pk_fma_f32 v[102:103], v[102:103], 2.0, 1.0 op_sel_hi:[1,0,0] neg_lo:[1,0,0] neg_hi:[1,0,0]
	v_pk_fma_f32 v[118:119], v[118:119], 2.0, 1.0 op_sel_hi:[1,0,0] neg_lo:[1,0,0] neg_hi:[1,0,0]
	v_add_f32_e32 v126, 1.0, v126
	v_add_f32_e32 v129, 1.0, v129
	v_add_f32_e32 v130, 1.0, v130
	v_add_f32_e32 v132, 1.0, v132
	v_fma_f32 v135, v149, -2.0, 1.0
	v_fma_f32 v141, v155, -2.0, 1.0
	v_pk_fma_f32 v[106:107], v[106:107], 2.0, 1.0 op_sel_hi:[1,0,0] neg_lo:[1,0,0] neg_hi:[1,0,0]
	v_add_f32_e32 v136, 1.0, v136
	v_pk_add_f32 v[100:101], v[100:101], 1.0 op_sel_hi:[1,0]
	v_pk_add_f32 v[102:103], v[102:103], 1.0 op_sel_hi:[1,0]
	v_pk_add_f32 v[118:119], v[118:119], 1.0 op_sel_hi:[1,0]
	v_mul_f32_e32 v126, v128, v126
	v_mul_f32_e32 v128, v150, v129
	v_mul_f32_e32 v129, v134, v130
	v_mul_f32_e32 v130, v152, v132
	v_fma_f32 v138, v153, -2.0, 1.0
	v_add_f32_e32 v135, 1.0, v135
	v_add_f32_e32 v141, 1.0, v141
	v_pk_add_f32 v[106:107], v[106:107], 1.0 op_sel_hi:[1,0]
	v_mul_f32_e32 v134, v154, v136
	v_pk_mul_f32 v[100:101], v[114:115], v[100:101]
	v_pk_mul_f32 v[102:103], v[116:117], v[102:103]
	v_pk_mul_f32 v[114:115], v[124:125], v[118:119]
	v_mul_f32_e32 v116, v127, v128
	v_mul_f32_e32 v118, v133, v130
	v_add_f32_e32 v138, 1.0, v138
	v_mul_f32_e32 v132, v140, v135
	v_mul_f32_e32 v136, v156, v141
	v_pk_mul_f32 v[106:107], v[122:123], v[106:107]
	v_mul_f32_e32 v113, v113, v126
	v_mul_f32_e32 v117, v131, v129
	v_mul_f32_e32 v122, v139, v134
	v_pk_mul_f32 v[98:99], v[98:99], v[114:115]
	v_mul_f32_e32 v114, v116, v116
	v_mul_f32_e32 v115, v118, v118
	v_mul_f32_e32 v135, v146, v138
	v_mul_f32_e32 v119, v137, v132
	v_mul_f32_e32 v124, v145, v136
	v_pk_mul_f32 v[96:97], v[96:97], v[102:103]
	v_pk_mul_f32 v[102:103], v[120:121], v[106:107]
	v_mul_f32_e32 v120, v122, v122
	v_fmac_f32_e32 v114, v113, v113
	v_fmac_f32_e32 v115, v117, v117
	v_mul_f32_e32 v123, v143, v135
	v_mul_f32_e32 v121, v124, v124
	v_fmac_f32_e32 v120, v119, v119
	v_add_f32_e32 v114, v114, v115
	v_pk_mul_f32 v[100:101], v[104:105], v[100:101]
	v_pk_mul_f32 v[104:105], v[96:97], v[96:97]
	v_fmac_f32_e32 v121, v123, v123
	v_add_f32_e32 v114, v120, v114
	v_pk_fma_f32 v[104:105], v[100:101], v[100:101], v[104:105]
	v_add_f32_e32 v114, v121, v114
	v_pk_mul_f32 v[106:107], v[98:99], v[98:99]
	v_add_f32_e32 v104, v104, v114
	v_pk_fma_f32 v[106:107], v[102:103], v[102:103], v[106:107]
	v_add_f32_e32 v104, v105, v104
	v_add_f32_e32 v104, v106, v104
	v_add_f32_e32 v104, v107, v104
	s_waitcnt lgkmcnt(0)
; __device__ __forceinline__ unsigned pk2(float lo, float hi) { unsigned r; asm volatile("v_cvt_pk_bf16_f32 %0, %1, %2" : "=v"(r) : "v"(lo), "v"(hi)); return r; }
; __device__ __forceinline__ void p4_item(Ctx& F, int item) {
;     ...
;         const int t = item * 64 + 8 * w + rr;
;         {
;             float o[16];
; #pragma unroll
;             for (int q = 0; q < 4; ++q) { const f32x4 v = *(const f32x4*)(reto + (size_t)t * RW + c0 + 4 * q); o[4 * q] = v.x; o[4 * q + 1] = v.y; o[4 * q + 2] = v.z; o[4 * q + 3] = v.w; }
;             float s = 0.f;
; #pragma unroll
;             for (int q = 0; q < 16; ++q) s += o[q];
;             s += __shfl_xor(s, 1); s += __shfl_xor(s, 2); s += __shfl_xor(s, 4);
;             const float mu = s * (1.0f / 128.0f); float vq = 0.f;
; #pragma unroll
;             for (int q = 0; q < 16; ++q) { o[q] -= mu; vq += o[q] * o[q]; }
;             vq += __shfl_xor(vq, 1); vq += __shfl_xor(vq, 2); vq += __shfl_xor(vq, 4);
;     ...
;             const float rstd = rsqrtf(wave_sum(ss) * (1.0f / LW) + EPS);
;             u32x4 w0, w1;
; #pragma unroll
;             for (int q = 0; q < 4; ++q) { w0[q] = pk2(o[2 * q] * rstd * beta_l[2 * q], o[2 * q + 1] * rstd * beta_l[2 * q + 1]); w1[q] = pk2(o[8 + 2 * q] * rstd * beta_l[8 + 2 * q], o[9 + 2 * q] * rstd * beta_l[9 + 2 * q]); }
;             *(u32x4*)(cat + (size_t)t * DM + RW + c0) = w0; *(u32x4*)(cat + (size_t)t * DM + RW + c0 + 8) = w1;
	s_nop 1
	v_add_f32_dpp v104, v104, v104 quad_perm:[1,0,3,2] row_mask:0xf bank_mask:0xf
	s_waitcnt lgkmcnt(0)
	s_nop 1
	v_add_f32_dpp v104, v104, v104 quad_perm:[2,3,0,1] row_mask:0xf bank_mask:0xf
	s_waitcnt lgkmcnt(0)
	s_nop 1
	v_add_f32_dpp v104, v104, v104 row_half_mirror row_mask:0xf bank_mask:0xf
	s_waitcnt lgkmcnt(0)
	s_nop 1
	v_add_f32_dpp v104, v104, v104 row_mirror row_mask:0xf bank_mask:0xf
	s_waitcnt lgkmcnt(0)
	s_nop 1
	v_add_f32_dpp v104, v104, v104 row_bcast:15 row_mask:0xa bank_mask:0xf
	s_waitcnt lgkmcnt(0)
	s_nop 1
	v_add_f32_dpp v104, v104, v104 row_bcast:31 row_mask:0xc bank_mask:0xf
	s_nop 1
	v_readlane_b32 s98, v104, 63
	s_nop 1
	v_mov_b32_e32 v104, s98
	v_fmamk_f32 v104, v104, 0x3a800000, v112
	v_mul_f32_e32 v105, 0x4b800000, v104
	v_cmp_gt_f32_e32 vcc, s62, v104
	s_nop 1
	v_cndmask_b32_e32 v104, v104, v105, vcc
	v_rsq_f32_e32 v104, v104
	s_nop 0
	v_mul_f32_e32 v105, 0x45800000, v104
	v_cndmask_b32_e32 v104, v104, v105, vcc
	v_mul_f32_e32 v100, v100, v104
	v_mul_f32_e32 v101, v101, v104
	v_mul_f32_e32 v102, v102, v104
	v_mul_f32_e32 v105, v113, v104
	v_mul_f32_e32 v106, v116, v104
	v_mul_f32_e32 v96, v96, v104
	v_mul_f32_e32 v107, v117, v104
	v_mul_f32_e32 v113, v118, v104
	v_mul_f32_e32 v97, v97, v104
	v_mul_f32_e32 v114, v119, v104
	v_mul_f32_e32 v115, v122, v104
	v_mul_f32_e32 v98, v98, v104
	v_mul_f32_e32 v116, v123, v104
	v_mul_f32_e32 v117, v124, v104
	v_mul_f32_e32 v103, v103, v104
	v_mul_f32_e32 v99, v99, v104
	v_mul_f32_e32 v100, v26, v100
	v_mul_f32_e32 v101, v28, v101
	v_mul_f32_e32 v102, v30, v102
	v_mul_f32_e32 v104, v18, v105
	v_mul_f32_e32 v105, v19, v106
	v_mul_f32_e32 v106, v27, v96
	v_mul_f32_e32 v107, v20, v107
	v_mul_f32_e32 v113, v21, v113
	v_mul_f32_e32 v118, v29, v97
	v_mul_f32_e32 v114, v22, v114
	v_mul_f32_e32 v115, v23, v115
	v_mul_f32_e32 v119, v31, v98
	v_mul_f32_e32 v116, v24, v116
	v_mul_f32_e32 v117, v25, v117
	v_mul_f32_e32 v103, v32, v103
	v_mul_f32_e32 v120, v33, v99
	v_cvt_pk_bf16_f32 v96, v104, v105
	v_cvt_pk_bf16_f32 v100, v100, v106
	v_cvt_pk_bf16_f32 v97, v107, v113
	v_cvt_pk_bf16_f32 v101, v101, v118
	v_cvt_pk_bf16_f32 v98, v114, v115
	v_cvt_pk_bf16_f32 v102, v102, v119
	v_cvt_pk_bf16_f32 v99, v116, v117
	v_cvt_pk_bf16_f32 v103, v103, v120
	global_store_dwordx4 v[88:89], v[96:99], off offset:2048
	global_store_dwordx4 v[88:89], v[100:103], off offset:2064
	global_load_dwordx4 v[96:99], v[90:91], off
	s_nop 0
	global_load_dwordx4 v[100:103], v[94:95], off offset:2048
	s_nop 0
	global_load_dwordx4 v[92:95], v[92:93], off offset:16
	s_nop 0
	global_load_dwordx4 v[104:107], v[90:91], off offset:16
	global_load_dwordx4 v[114:117], v[90:91], off offset:32
	s_nop 0
	global_load_dwordx4 v[88:91], v[90:91], off offset:48
	s_waitcnt vmcnt(5)
	v_add_f32_e32 v113, 0, v96
	v_add_f32_e32 v113, v97, v113
	v_add_f32_e32 v113, v98, v113
	v_add_f32_e32 v113, v99, v113
	s_waitcnt vmcnt(2)
	v_add_f32_e32 v113, v104, v113
	v_add_f32_e32 v113, v105, v113
	v_add_f32_e32 v113, v106, v113
	v_add_f32_e32 v113, v107, v113
	s_waitcnt vmcnt(1)
	v_add_f32_e32 v113, v114, v113
	v_lshlrev_b32_e32 v118, 16, v100
	v_add_f32_e32 v113, v115, v113
	v_and_b32_e32 v132, 0xffff0000, v95
	v_mul_f32_e32 v119, 0xbfb8aa3b, v118
	v_add_f32_e32 v113, v116, v113
	v_mul_f32_e32 v134, 0xbfb8aa3b, v132
	v_exp_f32_e32 v119, v119
	v_add_f32_e32 v113, v117, v113
	v_exp_f32_e32 v134, v134
	s_waitcnt vmcnt(0)
	v_add_f32_e32 v113, v88, v113
	v_add_f32_e32 v113, v89, v113
	v_add_f32_e32 v113, v90, v113
	v_add_f32_e32 v119, 1.0, v119
	v_add_f32_e32 v113, v91, v113
	v_add_f32_e32 v150, 1.0, v134
	v_rcp_f32_e32 v134, v119
	v_and_b32_e32 v122, 0xffff0000, v102
	v_and_b32_e32 v124, 0xffff0000, v103
	v_and_b32_e32 v120, 0xffff0000, v100
	v_and_b32_e32 v100, 0xffff0000, v101
	s_waitcnt lgkmcnt(0)
	s_nop 1
	v_add_f32_dpp v113, v113, v113 quad_perm:[1,0,3,2] row_mask:0xf bank_mask:0xf
	v_and_b32_e32 v126, 0xffff0000, v92
	v_and_b32_e32 v128, 0xffff0000, v93
	v_and_b32_e32 v130, 0xffff0000, v94
	v_mul_f32_e32 v121, 0xbfb8aa3b, v120
	s_waitcnt lgkmcnt(0)
	s_nop 1
	v_add_f32_dpp v113, v113, v113 quad_perm:[2,3,0,1] row_mask:0xf bank_mask:0xf
	v_mul_f32_e32 v123, 0xbfb8aa3b, v100
	v_mul_f32_e32 v129, 0xbfb8aa3b, v126
	v_mul_f32_e32 v131, 0xbfb8aa3b, v128
	v_mul_f32_e32 v125, 0xbfb8aa3b, v122
	s_waitcnt lgkmcnt(0)
	s_nop 1
	v_add_f32_dpp v113, v113, v113 row_half_mirror row_mask:0xf bank_mask:0xf
	v_fmamk_f32 v137, v113, 0xbc000000, v97
	v_fmamk_f32 v135, v113, 0xbc000000, v96
	v_mul_f32_e32 v96, v137, v137
	v_fmamk_f32 v97, v113, 0xbc000000, v98
	v_fmac_f32_e32 v96, v135, v135
	v_fmac_f32_e32 v99, 0xbc000000, v113
	v_fmac_f32_e32 v96, v97, v97
	v_fmamk_f32 v141, v113, 0xbc000000, v104
	v_fmac_f32_e32 v96, v99, v99
	v_fmamk_f32 v139, v113, 0xbc000000, v105
	v_fmac_f32_e32 v96, v141, v141
	v_mul_f32_e32 v140, 0x3c000000, v113
	v_fmamk_f32 v105, v113, 0xbc000000, v106
	v_fmac_f32_e32 v96, v139, v139
	v_fmac_f32_e32 v107, 0xbc000000, v113
	v_pk_add_f32 v[114:115], v[114:115], v[140:141] op_sel_hi:[1,0] neg_lo:[0,1] neg_hi:[0,1]
	v_fmac_f32_e32 v96, v105, v105
	v_pk_mul_f32 v[142:143], v[114:115], v[114:115]
	v_fmac_f32_e32 v96, v107, v107
	v_pk_add_f32 v[116:117], v[116:117], v[140:141] op_sel_hi:[1,0] neg_lo:[0,1] neg_hi:[0,1]
	v_add_f32_e32 v96, v142, v96
	v_pk_mul_f32 v[144:145], v[116:117], v[116:117]
	v_add_f32_e32 v96, v143, v96
	v_pk_add_f32 v[88:89], v[88:89], v[140:141] op_sel_hi:[1,0] neg_lo:[0,1] neg_hi:[0,1]
	v_add_f32_e32 v96, v144, v96
	v_pk_mul_f32 v[146:147], v[88:89], v[88:89]
	v_add_f32_e32 v96, v145, v96
	v_pk_add_f32 v[90:91], v[90:91], v[140:141] op_sel_hi:[1,0] neg_lo:[0,1] neg_hi:[0,1]
	v_add_f32_e32 v96, v146, v96
	v_pk_mul_f32 v[148:149], v[90:91], v[90:91]
	v_add_f32_e32 v96, v147, v96
	v_add_f32_e32 v96, v148, v96
	v_add_f32_e32 v96, v149, v96
	v_mul_f32_e32 v133, 0xbfb8aa3b, v130
	v_exp_f32_e32 v121, v121
	v_exp_f32_e32 v123, v123
	v_exp_f32_e32 v129, v129
	s_waitcnt lgkmcnt(0)
; __device__ __forceinline__ float bflo(unsigned w) { return __uint_as_float(w << 16); }
; __device__ __forceinline__ float bfhi(unsigned w) { return __uint_as_float(w & 0xffff0000u); }
; __device__ __forceinline__ float siluf_(float x) { return x * __builtin_amdgcn_rcpf(1.0f + __expf(-x)); }
; __device__ __forceinline__ void p4_item(Ctx& F, int item) {
;     ...
;             for (int q = 0; q < 16; ++q) { o[q] -= mu; vq += o[q] * o[q]; }
;             vq += __shfl_xor(vq, 1); vq += __shfl_xor(vq, 2); vq += __shfl_xor(vq, 4);
;             const float rs = rsqrtf(vq * (1.0f / 128.0f) + EPS);
;             const u32x4 g0 = *(const u32x4*)(proj + (size_t)t * NIN + 3 * RW + c0), g1 = *(const u32x4*)(proj + (size_t)t * NIN + 3 * RW + c0 + 8);
;             float ss = 0.f;
; #pragma unroll
;             for (int q = 0; q < 8; ++q) { const unsigned gw_ = (q < 4) ? g0[q & 3] : g1[q & 3]; const float ga = bflo(gw_), gb = bfhi(gw_);
;                 o[2 * q] = siluf_(ga) * (o[2 * q] * rs); o[2 * q + 1] = siluf_(gb) * (o[2 * q + 1] * rs); ss += o[2 * q] * o[2 * q] + o[2 * q + 1] * o[2 * q + 1]; }
;             const float rstd = rsqrtf(wave_sum(ss) * (1.0f / RW) + EPS);
	s_nop 1
	v_add_f32_dpp v96, v96, v96 quad_perm:[1,0,3,2] row_mask:0xf bank_mask:0xf
	v_exp_f32_e32 v131, v131
	v_exp_f32_e32 v125, v125
	v_exp_f32_e32 v133, v133
	v_mul_f32_e32 v127, 0xbfb8aa3b, v124
	s_waitcnt lgkmcnt(0)
	s_nop 1
	v_add_f32_dpp v96, v96, v96 quad_perm:[2,3,0,1] row_mask:0xf bank_mask:0xf
	v_exp_f32_e32 v127, v127
	v_add_f32_e32 v121, 1.0, v121
	v_add_f32_e32 v123, 1.0, v123
	v_add_f32_e32 v129, 1.0, v129
	s_waitcnt lgkmcnt(0)
	s_nop 1
	v_add_f32_dpp v96, v96, v96 row_half_mirror row_mask:0xf bank_mask:0xf
	v_fmamk_f32 v96, v96, 0x3c000000, v112
	v_mul_f32_e32 v104, 0x4b800000, v96
	v_cmp_gt_f32_e32 vcc, s62, v96
	v_add_f32_e32 v131, 1.0, v131
	v_add_f32_e32 v125, 1.0, v125
	v_cndmask_b32_e32 v96, v96, v104, vcc
	v_rsq_f32_e32 v96, v96
	v_add_f32_e32 v133, 1.0, v133
	v_rcp_f32_e32 v136, v121
	v_rcp_f32_e32 v98, v123
	v_mul_f32_e32 v104, 0x45800000, v96
	v_cndmask_b32_e32 v119, v96, v104, vcc
	v_pk_mul_f32 v[134:135], v[134:135], v[118:119]
	v_lshlrev_b32_e32 v118, 16, v101
	v_mul_f32_e32 v96, 0xbfb8aa3b, v118
	v_exp_f32_e32 v96, v96
	v_mov_b32_e32 v151, v114
	v_rcp_f32_e32 v114, v129
	v_mov_b32_e32 v153, v116
	v_add_f32_e32 v96, 1.0, v96
	v_rcp_f32_e32 v96, v96
	v_rcp_f32_e32 v116, v131
	v_rcp_f32_e32 v138, v125
	v_mov_b32_e32 v155, v88
	v_pk_mul_f32 v[96:97], v[96:97], v[118:119]
	v_lshlrev_b32_e32 v118, 16, v102
	v_mul_f32_e32 v102, v96, v97
	v_mul_f32_e32 v96, 0xbfb8aa3b, v118
	v_exp_f32_e32 v96, v96
	v_rcp_f32_e32 v88, v133
	v_mov_b32_e32 v157, v90
	v_rcp_f32_e32 v90, v150
	v_add_f32_e32 v96, 1.0, v96
	v_rcp_f32_e32 v140, v96
	v_add_f32_e32 v127, 1.0, v127
	v_rcp_f32_e32 v106, v127
	v_mov_b32_e32 v121, v119
	v_pk_mul_f32 v[96:97], v[140:141], v[118:119]
	v_lshlrev_b32_e32 v118, 16, v103
	v_mul_f32_e32 v103, v96, v97
	v_mul_f32_e32 v96, 0xbfb8aa3b, v118
	v_exp_f32_e32 v96, v96
	v_mov_b32_e32 v101, v119
	v_mov_b32_e32 v127, v119
	v_mov_b32_e32 v129, v119
	v_add_f32_e32 v96, 1.0, v96
	v_rcp_f32_e32 v104, v96
	v_mov_b32_e32 v123, v119
	v_mov_b32_e32 v131, v119
	v_mov_b32_e32 v133, v119
	v_pk_mul_f32 v[96:97], v[104:105], v[118:119]
	v_lshlrev_b32_e32 v118, 16, v92
	v_mul_f32_e32 v92, 0xbfb8aa3b, v118
	v_exp_f32_e32 v92, v92
	v_pk_mul_f32 v[120:121], v[136:137], v[120:121]
	v_pk_mul_f32 v[98:99], v[98:99], v[100:101]
	v_pk_mul_f32 v[114:115], v[114:115], v[126:127]
	v_pk_mul_f32 v[116:117], v[116:117], v[128:129]
	v_add_f32_e32 v92, 1.0, v92
	v_pk_mul_f32 v[100:101], v[138:139], v[122:123]
	v_pk_mul_f32 v[88:89], v[88:89], v[130:131]
	v_pk_mul_f32 v[90:91], v[90:91], v[132:133]
	v_mul_f32_e32 v120, v120, v121
	v_mul_f32_e32 v121, v98, v99
	v_mov_b32_e32 v98, v116
	v_mov_b32_e32 v99, v114
	v_mov_b32_e32 v114, v117
	v_rcp_f32_e32 v150, v92
	v_mul_f32_e32 v113, v134, v135
	v_mul_f32_e32 v122, v100, v101
	v_mov_b32_e32 v100, v90
	v_mov_b32_e32 v101, v88
	v_mov_b32_e32 v88, v91
	v_pk_mul_f32 v[90:91], v[98:99], v[114:115]
	v_mul_f32_e32 v98, v121, v121
	v_mul_f32_e32 v99, v120, v120
	v_pk_mul_f32 v[88:89], v[100:101], v[88:89]
	v_mul_f32_e32 v100, v122, v122
	v_fmac_f32_e32 v99, v113, v113
	v_fmac_f32_e32 v98, v102, v102
	v_add_f32_e32 v98, v99, v98
	v_fmac_f32_e32 v100, v103, v103
	v_add_f32_e32 v98, v100, v98
	v_mul_f32_e32 v100, v96, v97
	v_pk_mul_f32 v[96:97], v[150:151], v[118:119]
	v_lshlrev_b32_e32 v118, 16, v93
	v_mul_f32_e32 v92, 0xbfb8aa3b, v118
	v_exp_f32_e32 v92, v92
	v_mov_b32_e32 v125, v119
	v_pk_mul_f32 v[106:107], v[106:107], v[124:125]
	v_mov_b32_e32 v93, v96
	v_add_f32_e32 v92, 1.0, v92
	v_rcp_f32_e32 v152, v92
	v_mul_f32_e32 v106, v106, v107
	v_mul_f32_e32 v101, v106, v106
	v_fmac_f32_e32 v101, v100, v100
	v_add_f32_e32 v101, v101, v98
	v_pk_mul_f32 v[98:99], v[152:153], v[118:119]
	v_lshlrev_b32_e32 v118, 16, v94
	v_mul_f32_e32 v94, 0xbfb8aa3b, v118
	v_exp_f32_e32 v94, v94
	v_mov_b32_e32 v92, v98
	v_mov_b32_e32 v96, v99
	v_pk_mul_f32 v[92:93], v[92:93], v[96:97]
	v_add_f32_e32 v94, 1.0, v94
	v_rcp_f32_e32 v154, v94
	v_pk_mul_f32 v[96:97], v[92:93], v[92:93]
	s_nop 0
	v_pk_fma_f32 v[96:97], v[90:91], v[90:91], v[96:97]
	s_nop 0
	v_add_f32_e32 v97, v97, v101
	v_add_f32_e32 v101, v96, v97
	v_pk_mul_f32 v[96:97], v[154:155], v[118:119]
	v_lshlrev_b32_e32 v118, 16, v95
	v_mul_f32_e32 v94, 0xbfb8aa3b, v118
	v_exp_f32_e32 v94, v94
	v_mov_b32_e32 v95, v96
	v_add_f32_e32 v94, 1.0, v94
	v_rcp_f32_e32 v156, v94
	s_nop 0
	v_pk_mul_f32 v[98:99], v[156:157], v[118:119]
	s_nop 0
	v_mov_b32_e32 v94, v98
	v_mov_b32_e32 v96, v99
	v_pk_mul_f32 v[94:95], v[94:95], v[96:97]
	s_nop 0
	v_pk_mul_f32 v[96:97], v[94:95], v[94:95]
	s_nop 0
	v_pk_fma_f32 v[96:97], v[88:89], v[88:89], v[96:97]
	s_nop 0
	v_add_f32_e32 v97, v97, v101
	v_add_f32_e32 v96, v96, v97
	s_waitcnt lgkmcnt(0)
	s_nop 1
	v_add_f32_dpp v96, v96, v96 quad_perm:[1,0,3,2] row_mask:0xf bank_mask:0xf
	s_waitcnt lgkmcnt(0)
	s_nop 1
	v_add_f32_dpp v96, v96, v96 quad_perm:[2,3,0,1] row_mask:0xf bank_mask:0xf
	s_waitcnt lgkmcnt(0)
	s_nop 1
	v_add_f32_dpp v96, v96, v96 row_half_mirror row_mask:0xf bank_mask:0xf
	s_waitcnt lgkmcnt(0)
	s_nop 1
	v_add_f32_dpp v96, v96, v96 row_mirror row_mask:0xf bank_mask:0xf
	s_waitcnt lgkmcnt(0)
	s_nop 1
	v_add_f32_dpp v96, v96, v96 row_bcast:15 row_mask:0xa bank_mask:0xf
	s_waitcnt lgkmcnt(0)
; __device__ __forceinline__ unsigned pk2(float lo, float hi) { unsigned r; asm volatile("v_cvt_pk_bf16_f32 %0, %1, %2" : "=v"(r) : "v"(lo), "v"(hi)); return r; }
; __device__ __forceinline__ float bflo(unsigned w) { return __uint_as_float(w << 16); }
; __device__ __forceinline__ float bfhi(unsigned w) { return __uint_as_float(w & 0xffff0000u); }
; __device__ __forceinline__ float gelu_tanh_(float x) { const float u = 0.7978845608028654f * (x + 0.044715f * x * x * x); const float e = __expf(2.0f * u); const float th = 1.0f - 2.0f * __builtin_amdgcn_rcpf(e + 1.0f); return 0.5f * x * (1.0f + th); }
; __device__ __forceinline__ void p4_item(Ctx& F, int item) {
;     ...
;             const float rstd = rsqrtf(wave_sum(ss) * (1.0f / RW) + EPS);
;             u32x4 w0, w1;
; #pragma unroll
;             for (int q = 0; q < 4; ++q) { w0[q] = pk2(o[2 * q] * rstd * beta_r[2 * q], o[2 * q + 1] * rstd * beta_r[2 * q + 1]); w1[q] = pk2(o[8 + 2 * q] * rstd * beta_r[8 + 2 * q], o[9 + 2 * q] * rstd * beta_r[9 + 2 * q]); }
;             *(u32x4*)(cat + (size_t)t * DM + c0) = w0; *(u32x4*)(cat + (size_t)t * DM + c0 + 8) = w1;
;         }
;         {
;             const u32x4 h0 = *(const u32x4*)(hl + (size_t)t * LW + c0), h1 = *(const u32x4*)(hl + (size_t)t * LW + c0 + 8), p0 = *(const u32x4*)(pl + (size_t)t * LW + c0), p1 = *(const u32x4*)(pl + (size_t)t * LW + c0 + 8);
;             const u32x4 y0 = *(const u32x4*)(proj + (size_t)t * NIN + 5 * RW + c0), y1 = *(const u32x4*)(proj + (size_t)t * NIN + 5 * RW + c0 + 8);
;             float o[16]; float ss = 0.f;
; #pragma unroll
;             for (int q = 0; q < 8; ++q) { const unsigned hw = (q < 4) ? h0[q & 3] : h1[q & 3], pw = (q < 4) ? p0[q & 3] : p1[q & 3], yw = (q < 4) ? y0[q & 3] : y1[q & 3];
;                 const float ha = bflo(hw) + bflo(pw) * cr[2 * q], hb = bfhi(hw) + bfhi(pw) * cr[2 * q + 1];
;                 o[2 * q] = ha * gelu_tanh_(bflo(yw)); o[2 * q + 1] = hb * gelu_tanh_(bfhi(yw)); ss += o[2 * q] * o[2 * q] + o[2 * q + 1] * o[2 * q + 1]; }
	s_nop 1
	v_add_f32_dpp v96, v96, v96 row_bcast:31 row_mask:0xc bank_mask:0xf
	s_nop 1
	v_readlane_b32 s98, v96, 63
	s_nop 1
	v_mov_b32_e32 v96, s98
	v_fmamk_f32 v96, v96, 0x3a800000, v112
	v_mul_f32_e32 v97, 0x4b800000, v96
	v_cmp_gt_f32_e32 vcc, s62, v96
	s_nop 1
	v_cndmask_b32_e32 v96, v96, v97, vcc
	v_rsq_f32_e32 v96, v96
	s_nop 0
	v_mul_f32_e32 v97, 0x45800000, v96
	v_cndmask_b32_e32 v96, v96, v97, vcc
	v_mul_f32_e32 v97, v113, v96
	v_mul_f32_e32 v98, v120, v96
	v_mul_f32_e32 v93, v93, v96
	v_mul_f32_e32 v91, v91, v96
	v_mul_f32_e32 v99, v102, v96
	v_mul_f32_e32 v101, v121, v96
	v_mul_f32_e32 v90, v90, v96
	v_mul_f32_e32 v95, v95, v96
	v_mul_f32_e32 v92, v92, v96
	v_mul_f32_e32 v102, v103, v96
	v_mul_f32_e32 v103, v122, v96
	v_mul_f32_e32 v89, v89, v96
	v_mul_f32_e32 v100, v100, v96
	v_mul_f32_e32 v104, v106, v96
	v_mul_f32_e32 v94, v94, v96
	v_mul_f32_e32 v88, v88, v96
	v_mul_f32_e32 v96, v2, v97
	v_mul_f32_e32 v97, v3, v98
	v_mul_f32_e32 v93, v10, v93
	v_mul_f32_e32 v91, v11, v91
	v_mul_f32_e32 v98, v4, v99
	v_mul_f32_e32 v99, v5, v101
	v_mul_f32_e32 v90, v13, v90
	v_mul_f32_e32 v95, v14, v95
	v_mul_f32_e32 v101, v12, v92
	v_mul_f32_e32 v102, v6, v102
	v_mul_f32_e32 v103, v7, v103
	v_mul_f32_e32 v105, v15, v89
	v_mul_f32_e32 v100, v8, v100
	v_mul_f32_e32 v104, v9, v104
	v_mul_f32_e32 v106, v16, v94
	v_mul_f32_e32 v107, v17, v88
	v_cvt_pk_bf16_f32 v88, v96, v97
	v_cvt_pk_bf16_f32 v92, v93, v91
	v_cvt_pk_bf16_f32 v89, v98, v99
	v_cvt_pk_bf16_f32 v93, v101, v90
	v_cvt_pk_bf16_f32 v90, v102, v103
	v_cvt_pk_bf16_f32 v94, v95, v105
	v_cvt_pk_bf16_f32 v91, v100, v104
	v_cvt_pk_bf16_f32 v95, v106, v107
	global_load_dwordx4 v[96:99], v[86:87], off offset:2048
	s_nop 0
	global_load_dwordx4 v[84:87], v[84:85], off offset:16
	s_nop 0
	global_store_dwordx4 v[38:39], v[88:91], off
	global_store_dwordx4 v[38:39], v[92:95], off offset:16
	global_load_dwordx4 v[88:91], v[80:81], off
	s_nop 0
	global_load_dwordx4 v[92:95], v[82:83], off
	global_load_dwordx4 v[100:103], v[80:81], off offset:16
	s_nop 0
	global_load_dwordx4 v[80:83], v[82:83], off offset:16
	s_waitcnt vmcnt(7)
	v_lshlrev_b32_e32 v113, 16, v96
	v_and_b32_e32 v118, 0xffff0000, v96
	v_lshlrev_b32_e32 v119, 16, v97
	v_and_b32_e32 v120, 0xffff0000, v97
	v_lshlrev_b32_e32 v121, 16, v98
	v_and_b32_e32 v122, 0xffff0000, v98
	v_lshlrev_b32_e32 v123, 16, v99
	v_and_b32_e32 v124, 0xffff0000, v99
	s_waitcnt vmcnt(6)
	v_lshlrev_b32_e32 v97, 16, v85
	v_and_b32_e32 v85, 0xffff0000, v85
	v_lshlrev_b32_e32 v99, 16, v87
	v_lshlrev_b32_e32 v98, 16, v86
	v_mul_f32_e32 v125, 0x3d372713, v113
	v_mul_f32_e32 v127, 0x3d372713, v118
	v_mul_f32_e32 v129, 0x3d372713, v119
	v_mul_f32_e32 v131, 0x3d372713, v120
	v_lshlrev_b32_e32 v96, 16, v84
	v_and_b32_e32 v84, 0xffff0000, v84
	v_and_b32_e32 v87, 0xffff0000, v87
	v_and_b32_e32 v86, 0xffff0000, v86
	v_mul_f32_e32 v133, 0x3d372713, v121
	v_mul_f32_e32 v135, 0x3d372713, v122
	v_mul_f32_e32 v145, 0x3d372713, v97
	v_mul_f32_e32 v147, 0x3d372713, v85
	v_mul_f32_e32 v149, 0x3d372713, v98
	v_mul_f32_e32 v153, 0x3d372713, v99
	v_mul_f32_e32 v125, v125, v113
	v_mul_f32_e32 v127, v127, v118
	v_mul_f32_e32 v129, v129, v119
	v_mul_f32_e32 v131, v131, v120
	v_mul_f32_e32 v126, 0.5, v113
	v_mul_f32_e32 v128, 0.5, v118
	v_mul_f32_e32 v130, 0.5, v119
	v_mul_f32_e32 v137, 0x3d372713, v123
	v_mul_f32_e32 v139, 0x3d372713, v124
	v_mul_f32_e32 v141, 0x3d372713, v96
	v_mul_f32_e32 v143, 0x3d372713, v84
	v_mov_b32_e32 v146, v97
	v_pk_mul_f32 v[104:105], v[96:97], 0.5 op_sel_hi:[1,0]
	v_mov_b32_e32 v148, v85
	v_pk_mul_f32 v[106:107], v[84:85], 0.5 op_sel_hi:[1,0]
	v_mov_b32_e32 v150, v98
	v_mul_f32_e32 v151, 0x3d372713, v86
	v_mov_b32_e32 v154, v99
	v_pk_mul_f32 v[114:115], v[98:99], 0.5 op_sel_hi:[1,0]
	v_mul_f32_e32 v155, 0x3d372713, v87
	s_waitcnt vmcnt(3)
	v_lshlrev_b32_e32 v157, 16, v88
	s_waitcnt vmcnt(2)
	v_lshlrev_b32_e32 v158, 16, v92
	v_and_b32_e32 v159, 0xffff0000, v88
	v_and_b32_e32 v160, 0xffff0000, v92
	v_lshlrev_b32_e32 v161, 16, v89
	v_lshlrev_b32_e32 v162, 16, v93
	v_and_b32_e32 v163, 0xffff0000, v89
	v_and_b32_e32 v164, 0xffff0000, v93
	v_lshlrev_b32_e32 v165, 16, v90
	v_and_b32_e32 v167, 0xffff0000, v90
	v_mul_f32_e32 v133, v133, v121
	v_mul_f32_e32 v135, v135, v122
	v_lshlrev_b32_e32 v169, 16, v91
	v_and_b32_e32 v171, 0xffff0000, v91
	s_waitcnt vmcnt(1)
	v_lshlrev_b32_e32 v89, 16, v101
	v_lshlrev_b32_e32 v88, 16, v100
	s_waitcnt vmcnt(0)
; __device__ __forceinline__ float bflo(unsigned w) { return __uint_as_float(w << 16); }
; __device__ __forceinline__ float bfhi(unsigned w) { return __uint_as_float(w & 0xffff0000u); }
; __device__ __forceinline__ float gelu_tanh_(float x) { const float u = 0.7978845608028654f * (x + 0.044715f * x * x * x); const float e = __expf(2.0f * u); const float th = 1.0f - 2.0f * __builtin_amdgcn_rcpf(e + 1.0f); return 0.5f * x * (1.0f + th); }
; __device__ __forceinline__ void p4_item(Ctx& F, int item) {
;     ...
;             const u32x4 h0 = *(const u32x4*)(hl + (size_t)t * LW + c0), h1 = *(const u32x4*)(hl + (size_t)t * LW + c0 + 8), p0 = *(const u32x4*)(pl + (size_t)t * LW + c0), p1 = *(const u32x4*)(pl + (size_t)t * LW + c0 + 8);
;             const u32x4 y0 = *(const u32x4*)(proj + (size_t)t * NIN + 5 * RW + c0), y1 = *(const u32x4*)(proj + (size_t)t * NIN + 5 * RW + c0 + 8);
;             float o[16]; float ss = 0.f;
; #pragma unroll
;             for (int q = 0; q < 8; ++q) { const unsigned hw = (q < 4) ? h0[q & 3] : h1[q & 3], pw = (q < 4) ? p0[q & 3] : p1[q & 3], yw = (q < 4) ? y0[q & 3] : y1[q & 3];
;                 const float ha = bflo(hw) + bflo(pw) * cr[2 * q], hb = bfhi(hw) + bfhi(pw) * cr[2 * q + 1];
;                 o[2 * q] = ha * gelu_tanh_(bflo(yw)); o[2 * q + 1] = hb * gelu_tanh_(bfhi(yw)); ss += o[2 * q] * o[2 * q] + o[2 * q + 1] * o[2 * q + 1]; }
	v_lshlrev_b32_e32 v91, 16, v81
	v_lshlrev_b32_e32 v90, 16, v80
	v_and_b32_e32 v93, 0xffff0000, v101
	v_and_b32_e32 v92, 0xffff0000, v100
	v_mul_f32_e32 v100, v145, v97
	v_mul_f32_e32 v101, v147, v85
	v_mul_f32_e32 v98, v149, v98
	v_lshlrev_b32_e32 v85, 16, v103
	v_and_b32_e32 v97, 0xffff0000, v103
	v_mul_f32_e32 v99, v153, v99
	v_fma_f32 v103, v125, v113, v113
	v_fma_f32 v113, v127, v118, v118
	v_fma_f32 v118, v129, v119, v119
	v_fma_f32 v119, v131, v120, v120
	v_mul_f32_e32 v132, 0.5, v120
	v_mul_f32_e32 v134, 0.5, v121
	v_mov_b32_e32 v142, v96
	v_mov_b32_e32 v144, v84
	v_mov_b32_e32 v152, v86
	v_mov_b32_e32 v156, v87
	v_pk_mul_f32 v[116:117], v[86:87], 0.5 op_sel_hi:[1,0]
	v_mul_f32_e32 v137, v137, v123
	v_mul_f32_e32 v139, v139, v124
	v_mul_f32_e32 v141, v141, v96
	v_mul_f32_e32 v143, v143, v84
	v_and_b32_e32 v81, 0xffff0000, v81
	v_and_b32_e32 v80, 0xffff0000, v80
	v_mul_f32_e32 v145, v151, v86
	v_lshlrev_b32_e32 v84, 16, v102
	v_and_b32_e32 v96, 0xffff0000, v102
	v_mul_f32_e32 v102, v155, v87
	v_fma_f32 v120, v133, v121, v121
	v_fma_f32 v121, v135, v122, v122
	v_pk_fma_f32 v[86:87], v[34:35], v[90:91], v[88:89]
	v_fmac_f32_e32 v150, v98, v150
	v_fmac_f32_e32 v154, v99, v154
	v_mul_f32_e32 v89, 0x3f4c422a, v113
	v_mul_f32_e32 v91, 0x3f4c422a, v119
	v_mul_f32_e32 v136, 0.5, v122
	v_mul_f32_e32 v138, 0.5, v123
	v_lshlrev_b32_e32 v166, 16, v94
	v_and_b32_e32 v168, 0xffff0000, v94
	v_lshlrev_b32_e32 v170, 16, v95
	v_and_b32_e32 v172, 0xffff0000, v95
	v_lshlrev_b32_e32 v95, 16, v83
	v_lshlrev_b32_e32 v94, 16, v82
	v_fma_f32 v122, v137, v123, v123
	v_fma_f32 v123, v139, v124, v124
	v_pk_fma_f32 v[80:81], v[40:41], v[80:81], v[92:93]
	v_fmac_f32_e32 v146, v100, v146
	v_fmac_f32_e32 v152, v145, v152
	v_fmac_f32_e32 v156, v102, v156
	v_mul_f32_e32 v88, 0x3f4c422a, v103
	v_mul_f32_e32 v90, 0x3f4c422a, v118
	v_mul_f32_e32 v92, 0x3f4c422a, v120
	v_mul_f32_e32 v93, 0x3f4c422a, v121
	v_mul_f32_e32 v100, 0x3f4c422a, v150
	v_mul_f32_e32 v102, 0x3f4c422a, v154
	v_add_f32_e32 v89, v89, v89
	v_add_f32_e32 v91, v91, v91
	v_and_b32_e32 v83, 0xffff0000, v83
	v_and_b32_e32 v82, 0xffff0000, v82
	v_fmac_f32_e32 v144, v143, v144
	v_fmac_f32_e32 v148, v101, v148
	v_pk_fma_f32 v[84:85], v[78:79], v[94:95], v[84:85]
	v_mul_f32_e32 v94, 0x3f4c422a, v122
	v_mul_f32_e32 v95, 0x3f4c422a, v123
	v_mul_f32_e32 v101, 0x3f4c422a, v152
	v_mul_f32_e32 v103, 0x3f4c422a, v156
	v_add_f32_e32 v88, v88, v88
	v_add_f32_e32 v90, v90, v90
	v_add_f32_e32 v92, v92, v92
	v_add_f32_e32 v93, v93, v93
	v_add_f32_e32 v100, v100, v100
	v_add_f32_e32 v102, v102, v102
	v_mul_f32_e32 v89, 0x3fb8aa3b, v89
	v_mul_f32_e32 v91, 0x3fb8aa3b, v91
	v_fmac_f32_e32 v142, v141, v142
	v_pk_fma_f32 v[82:83], v[36:37], v[82:83], v[96:97]
	v_mul_f32_e32 v97, 0x3f4c422a, v144
	v_mul_f32_e32 v99, 0x3f4c422a, v148
	v_add_f32_e32 v94, v94, v94
	v_add_f32_e32 v95, v95, v95
	v_add_f32_e32 v101, v101, v101
	v_add_f32_e32 v103, v103, v103
	v_mul_f32_e32 v88, 0x3fb8aa3b, v88
	v_mul_f32_e32 v90, 0x3fb8aa3b, v90
	v_mul_f32_e32 v92, 0x3fb8aa3b, v92
	v_mul_f32_e32 v93, 0x3fb8aa3b, v93
	v_mul_f32_e32 v100, 0x3fb8aa3b, v100
	v_mul_f32_e32 v102, 0x3fb8aa3b, v102
	v_exp_f32_e32 v89, v89
	v_exp_f32_e32 v91, v91
	v_mul_f32_e32 v96, 0x3f4c422a, v142
	v_mul_f32_e32 v98, 0x3f4c422a, v146
	v_add_f32_e32 v97, v97, v97
	v_add_f32_e32 v99, v99, v99
	v_mul_f32_e32 v94, 0x3fb8aa3b, v94
	v_mul_f32_e32 v95, 0x3fb8aa3b, v95
	v_mul_f32_e32 v101, 0x3fb8aa3b, v101
	v_mul_f32_e32 v103, 0x3fb8aa3b, v103
	v_exp_f32_e32 v88, v88
	v_exp_f32_e32 v90, v90
	v_exp_f32_e32 v92, v92
	v_exp_f32_e32 v93, v93
	v_exp_f32_e32 v100, v100
	v_exp_f32_e32 v102, v102
	v_add_f32_e32 v96, v96, v96
	v_add_f32_e32 v98, v98, v98
	v_mul_f32_e32 v97, 0x3fb8aa3b, v97
	v_mul_f32_e32 v99, 0x3fb8aa3b, v99
	v_exp_f32_e32 v94, v94
	v_exp_f32_e32 v95, v95
	v_exp_f32_e32 v101, v101
	v_exp_f32_e32 v103, v103
	v_mul_f32_e32 v96, 0x3fb8aa3b, v96
	v_mul_f32_e32 v98, 0x3fb8aa3b, v98
	v_exp_f32_e32 v97, v97
	v_exp_f32_e32 v99, v99
	v_exp_f32_e32 v96, v96
	v_exp_f32_e32 v98, v98
	v_add_f32_e32 v89, 1.0, v89
	v_add_f32_e32 v91, 1.0, v91
	v_add_f32_e32 v88, 1.0, v88
	v_add_f32_e32 v90, 1.0, v90
	v_add_f32_e32 v92, 1.0, v92
	v_add_f32_e32 v93, 1.0, v93
	v_add_f32_e32 v100, 1.0, v100
	v_add_f32_e32 v102, 1.0, v102
	v_rcp_f32_e32 v118, v89
	v_rcp_f32_e32 v120, v91
	v_add_f32_e32 v94, 1.0, v94
	v_add_f32_e32 v95, 1.0, v95
	v_add_f32_e32 v101, 1.0, v101
	v_add_f32_e32 v103, 1.0, v103
	v_rcp_f32_e32 v113, v88
	v_rcp_f32_e32 v119, v90
	v_rcp_f32_e32 v121, v92
	v_rcp_f32_e32 v122, v93
	v_rcp_f32_e32 v92, v100
	v_rcp_f32_e32 v93, v102
	v_mul_f32_e32 v140, 0.5, v124
	v_add_f32_e32 v97, 1.0, v97
	v_add_f32_e32 v99, 1.0, v99
	v_rcp_f32_e32 v123, v94
	v_rcp_f32_e32 v124, v95
	v_rcp_f32_e32 v94, v101
	v_rcp_f32_e32 v95, v103
	v_add_f32_e32 v96, 1.0, v96
	v_add_f32_e32 v98, 1.0, v98
	v_rcp_f32_e32 v90, v97
	v_rcp_f32_e32 v91, v99
	v_rcp_f32_e32 v88, v96
	v_rcp_f32_e32 v89, v98
	v_fma_f32 v97, v118, -2.0, 1.0
	v_fma_f32 v99, v120, -2.0, 1.0
	v_fma_f32 v96, v113, -2.0, 1.0
	v_fma_f32 v98, v119, -2.0, 1.0
	v_fma_f32 v101, v122, -2.0, 1.0
; __device__ __forceinline__ unsigned pk2(float lo, float hi) { unsigned r; asm volatile("v_cvt_pk_bf16_f32 %0, %1, %2" : "=v"(r) : "v"(lo), "v"(hi)); return r; }
; __device__ __forceinline__ float bflo(unsigned w) { return __uint_as_float(w << 16); }
; __device__ __forceinline__ float bfhi(unsigned w) { return __uint_as_float(w & 0xffff0000u); }
; __device__ __forceinline__ float gelu_tanh_(float x) { const float u = 0.7978845608028654f * (x + 0.044715f * x * x * x); const float e = __expf(2.0f * u); const float th = 1.0f - 2.0f * __builtin_amdgcn_rcpf(e + 1.0f); return 0.5f * x * (1.0f + th); }
; __device__ __forceinline__ void p4_item(Ctx& F, int item) {
;     ...
;             for (int q = 0; q < 8; ++q) { const unsigned hw = (q < 4) ? h0[q & 3] : h1[q & 3], pw = (q < 4) ? p0[q & 3] : p1[q & 3], yw = (q < 4) ? y0[q & 3] : y1[q & 3];
;                 const float ha = bflo(hw) + bflo(pw) * cr[2 * q], hb = bfhi(hw) + bfhi(pw) * cr[2 * q + 1];
;                 o[2 * q] = ha * gelu_tanh_(bflo(yw)); o[2 * q + 1] = hb * gelu_tanh_(bfhi(yw)); ss += o[2 * q] * o[2 * q] + o[2 * q + 1] * o[2 * q + 1]; }
;             const float rstd = rsqrtf(wave_sum(ss) * (1.0f / LW) + EPS);
;             u32x4 w0, w1;
; #pragma unroll
;             for (int q = 0; q < 4; ++q) { w0[q] = pk2(o[2 * q] * rstd * beta_l[2 * q], o[2 * q + 1] * rstd * beta_l[2 * q + 1]); w1[q] = pk2(o[8 + 2 * q] * rstd * beta_l[8 + 2 * q], o[9 + 2 * q] * rstd * beta_l[9 + 2 * q]); }
;             *(u32x4*)(cat + (size_t)t * DM + RW + c0) = w0; *(u32x4*)(cat + (size_t)t * DM + RW + c0 + 8) = w1;
;         }
;     }
;     __syncthreads();
	v_pk_fma_f32 v[92:93], v[92:93], 2.0, 1.0 op_sel_hi:[1,0,0] neg_lo:[1,0,0] neg_hi:[1,0,0]
	v_add_f32_e32 v97, 1.0, v97
	v_add_f32_e32 v99, 1.0, v99
	v_fmac_f32_e32 v159, v43, v160
	v_fmac_f32_e32 v163, v45, v164
	v_fma_f32 v100, v121, -2.0, 1.0
	v_fma_f32 v103, v124, -2.0, 1.0
	v_pk_fma_f32 v[94:95], v[94:95], 2.0, 1.0 op_sel_hi:[1,0,0] neg_lo:[1,0,0] neg_hi:[1,0,0]
	v_add_f32_e32 v96, 1.0, v96
	v_add_f32_e32 v98, 1.0, v98
	v_add_f32_e32 v101, 1.0, v101
	v_pk_add_f32 v[92:93], v[92:93], 1.0 op_sel_hi:[1,0]
	v_mul_f32_e32 v97, v128, v97
	v_mul_f32_e32 v99, v132, v99
	v_fmac_f32_e32 v157, v42, v158
	v_fmac_f32_e32 v161, v44, v162
	v_fmac_f32_e32 v167, v47, v168
	v_fma_f32 v102, v123, -2.0, 1.0
	v_pk_fma_f32 v[90:91], v[90:91], 2.0, 1.0 op_sel_hi:[1,0,0] neg_lo:[1,0,0] neg_hi:[1,0,0]
	v_add_f32_e32 v100, 1.0, v100
	v_add_f32_e32 v103, 1.0, v103
	v_pk_add_f32 v[94:95], v[94:95], 1.0 op_sel_hi:[1,0]
	v_mul_f32_e32 v96, v126, v96
	v_mul_f32_e32 v98, v130, v98
	v_mul_f32_e32 v101, v136, v101
	v_pk_mul_f32 v[92:93], v[114:115], v[92:93]
	v_mul_f32_e32 v97, v159, v97
	v_mul_f32_e32 v99, v163, v99
	v_fmac_f32_e32 v165, v46, v166
	v_fmac_f32_e32 v171, v49, v172
	v_pk_fma_f32 v[88:89], v[88:89], 2.0, 1.0 op_sel_hi:[1,0,0] neg_lo:[1,0,0] neg_hi:[1,0,0]
	v_add_f32_e32 v102, 1.0, v102
	v_pk_add_f32 v[90:91], v[90:91], 1.0 op_sel_hi:[1,0]
	v_mul_f32_e32 v100, v134, v100
	v_mul_f32_e32 v103, v140, v103
	v_pk_mul_f32 v[94:95], v[116:117], v[94:95]
	v_mul_f32_e32 v96, v157, v96
	v_mul_f32_e32 v98, v161, v98
	v_mul_f32_e32 v101, v167, v101
	v_pk_mul_f32 v[84:85], v[84:85], v[92:93]
	v_mul_f32_e32 v92, v97, v97
	v_mul_f32_e32 v93, v99, v99
	v_fmac_f32_e32 v169, v48, v170
	v_pk_add_f32 v[88:89], v[88:89], 1.0 op_sel_hi:[1,0]
	v_mul_f32_e32 v102, v138, v102
	v_pk_mul_f32 v[90:91], v[106:107], v[90:91]
	v_mul_f32_e32 v100, v165, v100
	v_mul_f32_e32 v103, v171, v103
	v_pk_mul_f32 v[82:83], v[82:83], v[94:95]
	v_mul_f32_e32 v94, v101, v101
	v_fmac_f32_e32 v92, v96, v96
	v_fmac_f32_e32 v93, v98, v98
	v_pk_mul_f32 v[88:89], v[104:105], v[88:89]
	v_mul_f32_e32 v102, v169, v102
	v_pk_mul_f32 v[80:81], v[80:81], v[90:91]
	v_mul_f32_e32 v95, v103, v103
	v_fmac_f32_e32 v94, v100, v100
	v_add_f32_e32 v92, v92, v93
	v_pk_mul_f32 v[86:87], v[86:87], v[88:89]
	v_pk_mul_f32 v[88:89], v[80:81], v[80:81]
	v_fmac_f32_e32 v95, v102, v102
	v_add_f32_e32 v92, v94, v92
	v_pk_fma_f32 v[88:89], v[86:87], v[86:87], v[88:89]
	v_add_f32_e32 v92, v95, v92
	v_pk_mul_f32 v[90:91], v[82:83], v[82:83]
	v_add_f32_e32 v88, v88, v92
	v_pk_fma_f32 v[90:91], v[84:85], v[84:85], v[90:91]
	v_add_f32_e32 v88, v89, v88
	v_add_f32_e32 v88, v90, v88
	v_add_f32_e32 v88, v91, v88
	s_waitcnt lgkmcnt(0)
	s_nop 1
	v_add_f32_dpp v88, v88, v88 quad_perm:[1,0,3,2] row_mask:0xf bank_mask:0xf
	s_waitcnt lgkmcnt(0)
	s_nop 1
	v_add_f32_dpp v88, v88, v88 quad_perm:[2,3,0,1] row_mask:0xf bank_mask:0xf
	s_waitcnt lgkmcnt(0)
	s_nop 1
	v_add_f32_dpp v88, v88, v88 row_half_mirror row_mask:0xf bank_mask:0xf
	s_waitcnt lgkmcnt(0)
	s_nop 1
	v_add_f32_dpp v88, v88, v88 row_mirror row_mask:0xf bank_mask:0xf
	s_waitcnt lgkmcnt(0)
	s_nop 1
	v_add_f32_dpp v88, v88, v88 row_bcast:15 row_mask:0xa bank_mask:0xf
	s_waitcnt lgkmcnt(0)
	s_nop 1
	v_add_f32_dpp v88, v88, v88 row_bcast:31 row_mask:0xc bank_mask:0xf
	s_nop 1
	v_readlane_b32 s98, v88, 63
	s_nop 1
	v_mov_b32_e32 v88, s98
	v_fmamk_f32 v88, v88, 0x3a800000, v112
	v_mul_f32_e32 v89, 0x4b800000, v88
	v_cmp_gt_f32_e32 vcc, s62, v88
	s_nop 1
	v_cndmask_b32_e32 v88, v88, v89, vcc
	v_rsq_f32_e32 v88, v88
	s_nop 0
	v_mul_f32_e32 v89, 0x45800000, v88
	v_cndmask_b32_e32 v88, v88, v89, vcc
	v_mul_f32_e32 v86, v86, v88
	v_mul_f32_e32 v89, v96, v88
	v_mul_f32_e32 v90, v97, v88
	v_mul_f32_e32 v80, v80, v88
	v_mul_f32_e32 v91, v98, v88
	v_mul_f32_e32 v92, v99, v88
	v_mul_f32_e32 v87, v87, v88
	v_mul_f32_e32 v81, v81, v88
	v_mul_f32_e32 v93, v100, v88
	v_mul_f32_e32 v94, v101, v88
	v_mul_f32_e32 v84, v84, v88
	v_mul_f32_e32 v82, v82, v88
	v_mul_f32_e32 v95, v102, v88
	v_mul_f32_e32 v96, v103, v88
	v_mul_f32_e32 v85, v85, v88
	v_mul_f32_e32 v83, v83, v88
	v_mul_f32_e32 v86, v26, v86
	v_mul_f32_e32 v88, v18, v89
	v_mul_f32_e32 v89, v19, v90
	v_mul_f32_e32 v90, v27, v80
	v_mul_f32_e32 v91, v20, v91
	v_mul_f32_e32 v92, v21, v92
	v_mul_f32_e32 v87, v28, v87
	v_mul_f32_e32 v97, v29, v81
	v_mul_f32_e32 v93, v22, v93
	v_mul_f32_e32 v94, v23, v94
	v_mul_f32_e32 v98, v30, v84
	v_mul_f32_e32 v99, v31, v82
	v_mul_f32_e32 v95, v24, v95
	v_mul_f32_e32 v96, v25, v96
	v_mul_f32_e32 v100, v32, v85
	v_mul_f32_e32 v101, v33, v83
	v_cvt_pk_bf16_f32 v80, v88, v89
	v_cvt_pk_bf16_f32 v84, v86, v90
	v_cvt_pk_bf16_f32 v81, v91, v92
	v_cvt_pk_bf16_f32 v85, v87, v97
	v_cvt_pk_bf16_f32 v82, v93, v94
	v_cvt_pk_bf16_f32 v86, v98, v99
	v_cvt_pk_bf16_f32 v83, v95, v96
	v_cvt_pk_bf16_f32 v87, v100, v101
	global_store_dwordx4 v[38:39], v[80:83], off offset:2048
	global_store_dwordx4 v[38:39], v[84:87], off offset:2064
	s_cbranch_scc1 .LBB0_441
	s_add_i32 s72, s72, s84
	s_add_i32 s60, s60, s61
	s_add_i32 s40, s40, s61
	s_cmpk_gt_i32 s72, 0xff
	s_barrier
	s_cbranch_scc0 .LBB0_440
